# v87 + grid barrier: last XCD leader bumps all XGEN release words directly (16-lane atomic); the per-XCD relay hop (poll TOPGEN, then bump own XGEN) is gone
# speedup vs baseline: 1.0107x; 1.0091x over previous
.LBB0_71:
	s_or_b64 exec, exec, s[4:5]
	s_and_saveexec_b64 s[4:5], s[10:11]
	s_cbranch_execz .LBB0_73
	v_mov_b32_e32 v2, 1
	global_atomic_add v[0:1], v2, off
	s_add_u32 s100, s70, 0x3500
	v_cmp_eq_u32_e32 vcc, s100, v0
	s_cbranch_vccz .Lopt27_1
	s_mov_b64 s[100:101], exec
	s_mov_b64 exec, 0xffff
	v_mbcnt_lo_u32_b32 v2, -1, 0
	v_mbcnt_hi_u32_b32 v2, -1, v2
	v_lshlrev_b32_e32 v2, 8, v2
	v_add_u32_e32 v2, 0x2000, v2
	v_mov_b32_e32 v3, 1
	global_atomic_add v2, v3, s[70:71] offset:1024
	s_mov_b64 exec, s[100:101]
.Lopt27_1:
.LBB0_73:
	s_or_b64 exec, exec, s[4:5]
	s_mov_b64 s[4:5], exec
	v_mbcnt_lo_u32_b32 v0, s4, 0
	v_mbcnt_hi_u32_b32 v0, s5, v0
	v_cmp_eq_u32_e32 vcc, 0, v0
	s_waitcnt vmcnt(0)
	buffer_inv sc1
.LBB0_75:
	s_waitcnt vmcnt(0)
.LBB0_76:
	s_or_b64 exec, exec, s[0:1]
	s_waitcnt lgkmcnt(0)
	s_barrier
	s_getreg_b32 s0, hwreg(HW_REG_HW_ID, 0, 6)
	s_lshl_b32 s0, s0, 2
	s_add_i32 s0, s0, 0x27000
	v_mov_b32_e32 v0, s0
	ds_read_b32 v0, v0
	v_mov_b32_e32 v1, 0
	s_cmpk_lt_i32 s72, 0x240
	s_waitcnt lgkmcnt(0)
	v_readfirstlane_b32 s0, v0
	v_mbcnt_lo_u32_b32 v0, -1, v1
	v_mbcnt_hi_u32_b32 v0, -1, v0
	v_lshl_or_b32 v8, s0, 6, v0
	s_cselect_b64 s[0:1], -1, 0
	s_cmpk_gt_i32 s72, 0x23f
	v_readfirstlane_b32 s33, v8
	s_cbranch_scc1 .LBB0_78
	s_ashr_i32 s2, s72, 31
	s_lshr_b32 s2, s2, 29
	s_add_i32 s2, s72, s2
	s_ashr_i32 s3, s2, 3
	s_and_b32 s2, s2, -8
	s_sub_i32 s2, s72, s2
	s_cmp_lt_i32 s2, 0
	s_movk_i32 s4, 0x49
	s_cselect_b32 s4, s4, 0x48
	s_mul_i32 s2, s4, s2
	s_add_i32 s2, s2, s3
	s_mul_hi_i32 s3, s2, 0x38e38e39
	s_lshr_b32 s4, s3, 31
	s_ashr_i32 s3, s3, 4
	s_add_i32 s3, s3, s4
	s_lshl_b32 s4, s3, 3
	s_mulk_i32 s3, 0x48
	s_sub_i32 s2, s2, s3
	s_bfe_i32 s3, s2, 0x80000
	s_bfe_u32 s3, s3, 0x3000c
	s_add_i32 s3, s2, s3
	s_bfe_i32 s5, s3, 0x80000
	s_and_b32 s3, s3, 0xf8
	s_sub_i32 s2, s2, s3
	s_sext_i32_i16 s5, s5
	s_sext_i32_i8 s2, s2
	s_add_i32 s6, s4, s2
	s_ashr_i32 s2, s5, 3

.LBB0_221:
	s_or_b64 exec, exec, s[4:5]
	s_and_saveexec_b64 s[4:5], s[12:13]
	s_cbranch_execz .LBB0_223
	v_mov_b32_e32 v2, 1
	global_atomic_add v[0:1], v2, off
	s_add_u32 s100, s70, 0x3500
	v_cmp_eq_u32_e32 vcc, s100, v0
	s_cbranch_vccz .Lopt27_2
	s_mov_b64 s[100:101], exec
	s_mov_b64 exec, 0xffff
	v_mbcnt_lo_u32_b32 v2, -1, 0
	v_mbcnt_hi_u32_b32 v2, -1, v2
	v_lshlrev_b32_e32 v2, 8, v2
	v_add_u32_e32 v2, 0x2000, v2
	v_mov_b32_e32 v3, 1
	global_atomic_add v2, v3, s[70:71] offset:1024
	s_mov_b64 exec, s[100:101]

.LBB0_225:
	s_waitcnt vmcnt(0)
.LBB0_226:
	v_writelane_b32 v253, s40, 26
	s_nop 1
	v_writelane_b32 v253, s41, 27
	s_or_b64 exec, exec, s[0:1]
	s_add_u32 s0, s70, 0x760d500
	s_addc_u32 s1, s71, 0
	v_writelane_b32 v253, s0, 28
	s_waitcnt lgkmcnt(0)
	s_barrier
	v_writelane_b32 v253, s1, 29
	s_getreg_b32 s0, hwreg(HW_REG_HW_ID, 0, 6)
	s_lshl_b32 s0, s0, 2
	s_add_i32 s0, s0, 0x27000
	v_mov_b32_e32 v0, s0
	ds_read_b32 v0, v0
	v_mov_b32_e32 v2, 0
	v_mov_b32_e32 v1, 0
	s_waitcnt lgkmcnt(0)
	v_readfirstlane_b32 s0, v0
	v_mbcnt_lo_u32_b32 v0, -1, v2
	v_mbcnt_hi_u32_b32 v0, -1, v0
	v_lshl_or_b32 v0, s0, 6, v0
	s_lshl_b32 s0, s72, 3
	v_writelane_b32 v253, s0, 30
	v_ashrrev_i32_e32 v2, 6, v0
	v_add_u32_e32 v120, s0, v2
	v_readlane_b32 s0, v253, 2
	s_lshl_b32 s74, s0, 3
	s_movk_i32 s0, 0x2000
	v_readlane_b32 s1, v253, 3
	v_cmp_gt_i32_e32 vcc, s0, v120
	s_and_saveexec_b64 s[0:1], vcc
	s_cbranch_execz .LBB0_269
	s_movk_i32 s2, 0x2200
	v_lshlrev_b32_e32 v5, 3, v0
	v_mul_lo_u32 v2, v2, s2
	v_bfe_u32 v122, v0, 3, 3
	v_and_b32_e32 v123, 56, v5
	v_and_b32_e32 v5, 7, v0
	v_lshlrev_b32_e32 v6, 9, v0
	v_add_u32_e32 v3, 0, v2
	v_lshlrev_b32_e32 v5, 4, v5
	v_and_b32_e32 v6, 0x800, v6
	v_lshlrev_b32_e32 v7, 4, v0
	v_mul_u32_u24_e32 v8, 0x90, v122
	v_and_b32_e32 v121, 31, v0
	v_bfe_u32 v4, v0, 5, 1
	v_add_u32_e32 v6, v3, v6
	v_and_b32_e32 v7, 48, v7
	v_add3_u32 v124, v3, v5, v8
	v_lshlrev_b32_e32 v5, 6, v122
	s_add_u32 s11, s70, 0x210e500
	v_add3_u32 v125, v6, v7, v5
	v_mul_u32_u24_e32 v5, 0x90, v121
	v_lshlrev_b32_e32 v6, 4, v4
	s_addc_u32 s24, s71, 0
	v_add3_u32 v126, v3, v5, v6
	v_and_b32_e32 v5, 16, v0
	v_bfe_u32 v6, v0, 2, 2
	v_lshlrev_b32_e32 v0, 2, v0
	s_add_u32 s25, s70, 0x210e600
	v_and_or_b32 v6, v122, 4, v6
	v_and_or_b32 v0, v0, 12, v5
	s_addc_u32 s26, s71, 0
	v_lshlrev_b32_e32 v5, 6, v6
	v_lshlrev_b32_e32 v0, 1, v0
	s_add_u32 s27, s70, 0x210d900
	v_add3_u32 v127, v3, v5, v0
	v_lshlrev_b32_e32 v0, 2, v4
	s_addc_u32 s28, s71, 0
	v_lshlrev_b32_e32 v3, 2, v121
	v_lshlrev_b32_e32 v2, 3, v4
	s_add_u32 s29, s70, 0x210dd00
	v_sub_u32_e32 v129, v3, v0
	v_lshlrev_b32_e32 v3, 4, v121
	s_mov_b32 s3, 0
	s_addc_u32 s33, s71, 0
	v_sub_u32_e32 v128, v121, v0
	v_sub_u32_e32 v130, v3, v0
	s_mov_b64 s[4:5], 0
	s_movk_i32 s40, 0x1200
	s_movk_i32 s41, 0x900
	s_movk_i32 s42, 0xff7f
	s_mov_b32 s10, 0x3e38aa3b
	s_mov_b32 s43, 0xff800000
	s_movk_i32 s44, 0xff7e
	s_movk_i32 s45, 0x81
	v_lshlrev_b32_e32 v114, 1, v0
	v_lshlrev_b32_e32 v116, 1, v2
	v_mov_b32_e32 v131, 0xff800000
	v_mov_b32_e32 v132, 0x1200
	s_branch .LBB0_231

.LBB0_320:
	s_waitcnt vmcnt(0)
.LBB0_321:
	v_writelane_b32 v253, s76, 31
	s_nop 1
	v_writelane_b32 v253, s77, 32
	v_writelane_b32 v253, s78, 33
	v_writelane_b32 v253, s79, 34
	v_writelane_b32 v253, s80, 35
	v_writelane_b32 v253, s81, 36
	v_writelane_b32 v253, s82, 37
	v_writelane_b32 v253, s83, 38
	v_writelane_b32 v253, s84, 39
	v_writelane_b32 v253, s85, 40
	v_writelane_b32 v253, s86, 41
	v_writelane_b32 v253, s87, 42
	v_writelane_b32 v253, s88, 43
	v_writelane_b32 v253, s89, 44
	v_writelane_b32 v253, s90, 45
	v_writelane_b32 v253, s91, 46
	s_or_b64 exec, exec, s[0:1]
	s_add_u32 s0, s70, 0xd400
	s_addc_u32 s1, s71, 0
	v_writelane_b32 v253, s0, 47
	s_waitcnt lgkmcnt(0)
	s_barrier
	v_writelane_b32 v253, s1, 48
	s_add_u32 s0, s70, 0x960d500
	s_addc_u32 s1, s71, 0
	s_add_u32 s92, s70, 0xd60d500
	v_writelane_b32 v253, s0, 49
	s_addc_u32 s93, s71, 0
	s_nop 0
	v_writelane_b32 v253, s1, 50
	s_add_u32 s0, s70, 0xf60d500
	s_addc_u32 s1, s71, 0
	v_writelane_b32 v253, s0, 51
	s_nop 1
	v_writelane_b32 v253, s1, 52
	s_getreg_b32 s0, hwreg(HW_REG_HW_ID, 0, 6)
	s_lshl_b32 s0, s0, 2
	s_add_i32 s0, s0, 0x27000
	v_mov_b32_e32 v0, s0
	ds_read_b32 v133, v0
	v_readlane_b32 s2, v253, 24
	v_readlane_b32 s3, v253, 25
	s_mov_b64 s[0:1], -1
	s_and_b64 vcc, exec, s[2:3]
	s_cbranch_vccz .LBB0_402
	v_mov_b32_e32 v0, 0
	s_waitcnt lgkmcnt(0)
	v_readfirstlane_b32 s0, v133
	v_mbcnt_lo_u32_b32 v0, -1, v0
	v_mbcnt_hi_u32_b32 v0, -1, v0
	v_lshl_or_b32 v8, s0, 6, v0
	v_mov_b32_e32 v146, 0
	s_cmpk_gt_i32 s72, 0xff
	v_readfirstlane_b32 s5, v8
	s_cbranch_scc1 .LBB0_342
	s_ashr_i32 s26, s72, 31
	s_lshr_b32 s0, s26, 29
	s_add_i32 s2, s72, s0
	s_and_b32 s0, s2, -8
	s_sub_i32 s4, s72, s0
	s_cmp_gt_i32 s4, -1
	s_cbranch_scc0 .LBB0_325
	s_lshl_b32 s3, s4, 5
	s_cbranch_execz .LBB0_326
	s_branch .LBB0_327

.LBB0_393:
	s_waitcnt vmcnt(0)
.LBB0_394:
	s_or_b64 exec, exec, s[0:1]
	s_waitcnt lgkmcnt(0)
	s_barrier
	s_getreg_b32 s0, hwreg(HW_REG_HW_ID, 0, 6)
	s_lshl_b32 s0, s0, 2
	s_add_i32 s0, s0, 0x27000
	v_mov_b32_e32 v0, s0
	ds_read_b32 v0, v0
	v_mov_b32_e32 v1, 0
	s_movk_i32 s24, 0x4000
	v_mov_b32_e32 v33, 0
	s_waitcnt lgkmcnt(0)
	v_readfirstlane_b32 s0, v0
	v_mbcnt_lo_u32_b32 v0, -1, v1
	v_mbcnt_hi_u32_b32 v0, -1, v0
	v_lshl_or_b32 v34, s0, 6, v0
	s_getreg_b32 s0, hwreg(HW_REG_HW_ID, 0, 6)
	s_lshl_b32 s0, s0, 2
	s_add_i32 s0, s0, 0x27000
	v_mov_b32_e32 v0, s0
	ds_read_b32 v0, v0
	v_mov_b32_e32 v1, 0
	s_waitcnt lgkmcnt(0)
	v_readfirstlane_b32 s0, v0
	v_mbcnt_lo_u32_b32 v0, -1, v1
	v_mbcnt_hi_u32_b32 v0, -1, v0
	v_lshl_or_b32 v0, s0, 6, v0
	v_readlane_b32 s0, v253, 30
	v_ashrrev_i32_e32 v0, 6, v0
	s_waitcnt vmcnt(12)
	v_add_u32_e32 v80, s0, v0
	v_cmp_gt_i32_e32 vcc, s24, v80
	s_and_saveexec_b64 s[10:11], vcc
	s_cbranch_execz .LBB0_401
	v_lshlrev_b32_e32 v0, 3, v34
	v_and_b32_e32 v35, 0x1f8, v0
	v_readlane_b32 s40, v253, 31
	v_lshlrev_b32_e32 v32, 2, v35
	v_readlane_b32 s50, v253, 41
	v_readlane_b32 s51, v253, 42
	v_readlane_b32 s52, v253, 43
	v_readlane_b32 s53, v253, 44
	s_nop 2
	global_load_dwordx4 v[0:3], v32, s[50:51] offset:16
	s_nop 0
	global_load_dwordx4 v[4:7], v32, s[52:53] offset:16
	global_load_dwordx4 v[8:11], v32, s[50:51]
	global_load_dwordx4 v[12:15], v32, s[52:53]
	global_load_dwordx4 v[16:19], v32, s[50:51] offset:2064
	global_load_dwordx4 v[20:23], v32, s[52:53] offset:2064
	global_load_dwordx4 v[24:27], v32, s[50:51] offset:2048
	global_load_dwordx4 v[28:31], v32, s[52:53] offset:2048
	v_readlane_b32 s2, v253, 49
	v_readlane_b32 s3, v253, 50
	v_ashrrev_i32_e32 v81, 31, v80
	s_waitcnt vmcnt(18)
	v_lshlrev_b64 v[90:91], 12, v[80:81]
	v_lshl_add_u64 v[82:83], s[2:3], 0, v[32:33]
	v_readlane_b32 s2, v253, 51
	v_lshlrev_b32_e32 v32, 1, v35
	v_readlane_b32 s3, v253, 52
	v_lshl_add_u64 v[84:85], s[92:93], 0, v[32:33]
	v_readlane_b32 s0, v253, 2
	v_lshl_add_u64 v[86:87], s[2:3], 0, v[32:33]
	v_and_b32_e32 v32, 63, v34
	v_lshlrev_b32_e32 v34, 4, v32
	v_lshl_or_b32 v90, v32, 5, v90
	v_add_u32_e32 v32, s74, v80
	s_lshl_b32 s12, s0, 5
	v_ashrrev_i32_e32 v33, 31, v32
	v_lshlrev_b64 v[88:89], 11, v[80:81]
	s_ashr_i32 s13, s12, 31
	s_waitcnt vmcnt(17)
	v_lshlrev_b64 v[92:93], 11, v[32:33]
	v_or_b32_e32 v88, v88, v34
	s_lshl_b64 s[14:15], s[12:13], 11
	s_lshl_b64 s[16:17], s[12:13], 12
	s_lshl_b32 s13, s0, 4
	s_mul_i32 s25, s0, 24
	v_or_b32_e32 v92, v92, v34
	s_mov_b64 s[18:19], 0
	s_mov_b64 s[20:21], 0x960d500
	s_mov_b64 s[22:23], 0x960dd00
	s_mov_b32 s26, 0x960d000
	v_mov_b32_e32 v81, 0x3727c5ac
	s_mov_b32 s27, 0x800000
	s_mov_b32 s28, 0xd60d000
	s_mov_b32 s29, 0xf60d000
	s_movk_i32 s33, 0x3fff
	v_readlane_b32 s41, v253, 32
	v_readlane_b32 s42, v253, 33
	v_readlane_b32 s43, v253, 34
	v_readlane_b32 s44, v253, 35
	v_readlane_b32 s45, v253, 36
	v_readlane_b32 s46, v253, 37
	v_readlane_b32 s47, v253, 38
	v_readlane_b32 s48, v253, 39
	v_readlane_b32 s49, v253, 40
	v_readlane_b32 s54, v253, 45
	v_readlane_b32 s55, v253, 46
	v_readlane_b32 s1, v253, 3
	s_branch .LBB0_397

.LBB0_518:
	s_waitcnt vmcnt(0)
.LBB0_519:
	s_or_b64 exec, exec, s[0:1]
	s_waitcnt lgkmcnt(0)
	s_barrier
	s_getreg_b32 s0, hwreg(HW_REG_HW_ID, 0, 6)
	s_lshl_b32 s0, s0, 2
	s_add_i32 s0, s0, 0x27000
	v_mov_b32_e32 v0, s0
	ds_read_b32 v0, v0
	v_mov_b32_e32 v1, 0
	s_movk_i32 s8, 0x100
	s_mov_b32 s9, s72
	s_waitcnt lgkmcnt(0)
	v_readfirstlane_b32 s0, v0
	v_mbcnt_lo_u32_b32 v0, -1, v1
	v_mbcnt_hi_u32_b32 v0, -1, v0
	v_lshl_or_b32 v0, s0, 6, v0
	v_readlane_b32 s0, v253, 2
	s_mov_b32 s2, s0
	s_and_b32 s0, s0, 7
	s_cmp_eq_u32 s0, 0
	s_cselect_b64 s[42:43], -1, 0
	s_cmp_lg_u32 s0, 0
	s_mov_b32 s10, s2
	v_readlane_b32 s1, v253, 3
	s_cbranch_scc1 .LBB0_521
	s_and_b32 s0, s72, 7
	s_lshl_b32 s1, s0, 5
	s_lshl_b32 s0, s0, 8
	s_lshr_b32 s2, s72, 3
	s_addk_i32 s0, 0x100
	s_add_i32 s9, s1, s2
	s_lshr_b32 s8, s0, 3
	v_readlane_b32 s0, v253, 2
	s_lshr_b32 s10, s0, 3
	v_readlane_b32 s1, v253, 3

.LBB0_573:
	s_or_b64 exec, exec, s[4:5]
	s_and_saveexec_b64 s[4:5], s[8:9]
	s_cbranch_execz .LBB0_575
	v_mov_b32_e32 v2, 1
	global_atomic_add v[0:1], v2, off
	s_add_u32 s100, s70, 0x3500
	v_cmp_eq_u32_e32 vcc, s100, v0
	s_cbranch_vccz .Lopt27_6
	s_mov_b64 s[100:101], exec
	s_mov_b64 exec, 0xffff
	v_mbcnt_lo_u32_b32 v2, -1, 0
	v_mbcnt_hi_u32_b32 v2, -1, v2
	v_lshlrev_b32_e32 v2, 8, v2
	v_add_u32_e32 v2, 0x2000, v2
	v_mov_b32_e32 v3, 1
	global_atomic_add v2, v3, s[70:71] offset:1024
	s_mov_b64 exec, s[100:101]

.LBB0_577:
	s_waitcnt vmcnt(0)
.LBB0_578:
	s_or_b64 exec, exec, s[0:1]
	s_add_u32 s40, s70, 0x5440
	s_addc_u32 s41, s71, 0
	s_add_u32 s0, s70, 0x1260d500
	s_addc_u32 s1, s71, 0
	v_writelane_b32 v253, s0, 55
	s_waitcnt lgkmcnt(0)
	s_barrier
	v_writelane_b32 v253, s1, 56
	s_add_u32 s0, s70, 0x1268d500
	s_addc_u32 s1, s71, 0
	v_writelane_b32 v253, s0, 57
	v_mov_b32_e32 v1, 0
	s_nop 0
	v_writelane_b32 v253, s1, 58
	s_add_u32 s0, s70, 0x1270d500
	s_addc_u32 s1, s71, 0
	v_writelane_b32 v253, s0, 59
	v_mov_b32_e32 v3, 0
	s_movk_i32 s33, 0x4000
	v_writelane_b32 v253, s1, 60
	s_add_u32 s0, s70, 0x1278d500
	s_addc_u32 s1, s71, 0
	v_writelane_b32 v253, s0, 61
	s_nop 1
	v_writelane_b32 v253, s1, 62
	s_getreg_b32 s0, hwreg(HW_REG_HW_ID, 0, 6)
	s_lshl_b32 s0, s0, 2
	s_add_i32 s0, s0, 0x27000
	v_mov_b32_e32 v0, s0
	ds_read_b32 v0, v0
	s_waitcnt lgkmcnt(0)
	v_readfirstlane_b32 s0, v0
	v_mbcnt_lo_u32_b32 v0, -1, v1
	v_mbcnt_hi_u32_b32 v0, -1, v0
	v_lshl_or_b32 v0, s0, 6, v0
	s_getreg_b32 s0, hwreg(HW_REG_HW_ID, 0, 6)
	s_lshl_b32 s0, s0, 2
	s_add_i32 s0, s0, 0x27000
	v_mov_b32_e32 v1, s0
	ds_read_b32 v2, v1
	v_mov_b32_e32 v1, 0
	s_waitcnt lgkmcnt(0)
	v_readfirstlane_b32 s0, v2
	v_mbcnt_lo_u32_b32 v2, -1, v3
	v_mbcnt_hi_u32_b32 v2, -1, v2
	v_lshl_or_b32 v2, s0, 6, v2
	v_readlane_b32 s0, v253, 30
	v_ashrrev_i32_e32 v8, 6, v2
	s_nop 0
	v_add_u32_e32 v2, s0, v8
	v_cmp_gt_i32_e32 vcc, s33, v2
	s_and_saveexec_b64 s[44:45], vcc
	s_cbranch_execz .LBB0_667
	v_ashrrev_i32_e32 v3, 31, v2
	v_readlane_b32 s2, v253, 53
	v_and_b32_e32 v22, 63, v0
	v_lshlrev_b64 v[4:5], 10, v[2:3]
	v_readlane_b32 s3, v253, 54
	v_lshlrev_b32_e32 v0, 2, v22
	v_readlane_b32 s12, v253, 4
	v_lshl_add_u64 v[4:5], s[2:3], 0, v[4:5]
	v_lshl_add_u64 v[4:5], v[4:5], 0, v[0:1]
	global_load_dword v24, v[4:5], off
	global_load_dword v29, v[4:5], off offset:256
	global_load_dword v30, v[4:5], off offset:512
	global_load_dword v9, v[4:5], off offset:768
	v_readlane_b32 s13, v253, 5
	v_xor_b32_e32 v3, 64, v0
	v_xor_b32_e32 v23, 0x80, v0
	v_lshl_add_u64 v[4:5], s[12:13], 0, v[0:1]
	global_load_dword v61, v[4:5], off
	global_load_dword v62, v[4:5], off offset:256
	global_load_dword v63, v[4:5], off offset:512
	global_load_dword v64, v[4:5], off offset:768
	v_lshl_add_u64 v[6:7], s[2:3], 0, v[0:1]
	s_lshl_b32 s2, s72, 6
	v_lshlrev_b32_e32 v0, 3, v8
	v_readlane_b32 s14, v253, 6
	v_readlane_b32 s15, v253, 7
	v_readlane_b32 s16, v253, 8
	v_readlane_b32 s17, v253, 9
	v_readlane_b32 s18, v253, 10
	v_readlane_b32 s19, v253, 11
	v_readlane_b32 s20, v253, 12
	v_readlane_b32 s21, v253, 13
	v_readlane_b32 s22, v253, 14
	v_readlane_b32 s23, v253, 15
	v_readlane_b32 s24, v253, 16
	v_readlane_b32 s25, v253, 17
	v_add3_u32 v8, s2, v0, v22
	v_readlane_b32 s2, v253, 2
	v_cmp_gt_u32_e64 s[0:1], 32, v22
	v_cmp_lt_u32_e64 s[4:5], 31, v22
	v_cmp_lt_u32_e64 s[6:7], 7, v22
	v_cmp_gt_u32_e64 s[8:9], 8, v22
	v_cmp_eq_u32_e64 s[10:11], 0, v22
	v_cmp_eq_u32_e64 s[12:13], 1, v22
	v_cmp_eq_u32_e64 s[14:15], 2, v22
	v_cmp_eq_u32_e64 s[16:17], 3, v22
	v_cmp_eq_u32_e64 s[18:19], 4, v22
	v_cmp_eq_u32_e64 s[20:21], 5, v22
	v_cmp_eq_u32_e64 s[22:23], 6, v22
	v_cmp_eq_u32_e64 s[24:25], 7, v22
	s_lshl_b32 s52, s2, 6
	s_mov_b64 s[46:47], 0
	s_mov_b32 s53, 0xbfb8aa3b
	s_mov_b32 s54, 0x42ce8ed0
	s_mov_b32 s55, 0xc2b17218
	v_mov_b32_e32 v25, 0x7f800000
	v_mov_b32_e32 v26, 0xff800000
	v_mov_b32_e32 v27, 1
	v_readlane_b32 s26, v253, 18
	v_readlane_b32 s27, v253, 19
	v_readlane_b32 s3, v253, 3
	s_waitcnt vmcnt(0)
	s_branch .LBB0_581

.LBB0_718:
	s_waitcnt vmcnt(0)
.LBB0_719:
	s_or_b64 exec, exec, s[0:1]
	s_waitcnt lgkmcnt(0)
	s_barrier
	s_getreg_b32 s0, hwreg(HW_REG_HW_ID, 0, 6)
	s_lshl_b32 s0, s0, 2
	s_add_i32 s0, s0, 0x27000
	v_mov_b32_e32 v0, s0
	ds_read_b32 v0, v0
	v_mov_b32_e32 v1, 0
	v_mov_b32_e32 v2, 0
	s_waitcnt lgkmcnt(0)
	v_readfirstlane_b32 s0, v0
	v_mbcnt_lo_u32_b32 v0, -1, v1
	v_mbcnt_hi_u32_b32 v0, -1, v0
	s_waitcnt vmcnt(9)
	v_lshl_or_b32 v52, s0, 6, v0
	s_getreg_b32 s0, hwreg(HW_REG_HW_ID, 0, 6)
	s_lshl_b32 s0, s0, 2
	s_add_i32 s0, s0, 0x27000
	v_mov_b32_e32 v0, s0
	ds_read_b32 v0, v0
	v_mov_b32_e32 v1, 0
	s_waitcnt lgkmcnt(0)
	v_readfirstlane_b32 s0, v0
	v_mbcnt_lo_u32_b32 v0, -1, v2
	v_mbcnt_hi_u32_b32 v0, -1, v0
	v_lshl_or_b32 v0, s0, 6, v0
	s_movk_i32 s0, 0x100
	s_nop 0
	v_cmp_gt_i32_e32 vcc, s0, v0
	v_lshl_add_u32 v2, v0, 2, 0
	s_and_saveexec_b64 s[0:1], vcc
	s_cbranch_execz .LBB0_721
	v_ashrrev_i32_e32 v1, 31, v0
	v_lshlrev_b32_e32 v4, 6, v0
	v_and_b32_e32 v4, 0xffffff00, v4
	v_and_b32_e32 v5, 3, v0
	v_lshl_or_b32 v4, v5, 5, v4
	v_mov_b32_e32 v5, 0
	v_lshl_add_u64 v[4:5], v[4:5], 0, s[40:41]
	global_load_dword v1, v[4:5], off
	v_add_u32_e32 v3, 0x1e800, v2
	s_mov_b32 s2, 0x66666667
	s_waitcnt vmcnt(0)
	ds_write_b32 v3, v1
	v_add_u32_e32 v3, 0x13f, v1
	v_mul_hi_i32 v3, v3, s2
	v_lshrrev_b32_e32 v4, 31, v3
	v_lshrrev_b32_e32 v3, 7, v3
	v_add_u32_e32 v3, v3, v4
	v_lshl_or_b32 v1, v3, 20, v1
	v_add_u32_e32 v3, 0x1ec10, v2
	ds_write_b32 v3, v1

.LBB0_854:
	s_waitcnt vmcnt(0)
.LBB0_855:
	s_or_b64 exec, exec, s[0:1]
	s_waitcnt lgkmcnt(0)
	s_barrier
	s_getreg_b32 s0, hwreg(HW_REG_HW_ID, 0, 6)
	s_lshl_b32 s0, s0, 2
	s_add_i32 s0, s0, 0x27000
	v_mov_b32_e32 v0, s0
	ds_read_b32 v0, v0
	v_mov_b32_e32 v1, 0
	v_mov_b32_e32 v2, 0
	s_waitcnt lgkmcnt(0)
	v_readfirstlane_b32 s0, v0
	v_mbcnt_lo_u32_b32 v0, -1, v1
	v_mbcnt_hi_u32_b32 v0, -1, v0
	v_lshl_or_b32 v52, s0, 6, v0
	s_getreg_b32 s0, hwreg(HW_REG_HW_ID, 0, 6)
	s_lshl_b32 s0, s0, 2
	s_add_i32 s0, s0, 0x27000
	v_mov_b32_e32 v0, s0
	ds_read_b32 v0, v0
	v_mov_b32_e32 v1, 0
	s_waitcnt lgkmcnt(0)
	v_readfirstlane_b32 s0, v0
	v_mbcnt_lo_u32_b32 v0, -1, v2
	v_mbcnt_hi_u32_b32 v0, -1, v0
	v_lshl_or_b32 v0, s0, 6, v0
	s_movk_i32 s0, 0x100
	s_nop 0
	v_cmp_gt_i32_e32 vcc, s0, v0
	v_lshl_add_u32 v2, v0, 2, 0
	s_add_i32 s0, 0, 0x1f424
	v_mov_b32_e32 v0, s0
	s_waitcnt lgkmcnt(0)
	s_barrier
	ds_read_b32 v0, v0
	v_readlane_b32 s2, v253, 63
	v_readlane_b32 s3, v254, 0
	s_and_b64 vcc, exec, s[2:3]
	s_waitcnt lgkmcnt(0)
	v_readfirstlane_b32 s0, v0
	s_lshl_b32 s0, s0, 3
	s_cbranch_vccz .LBB0_896
	v_readlane_b32 s2, v253, 2
	s_mov_b32 s12, s72
	v_readlane_b32 s3, v253, 3
	s_mov_b32 s1, s2
	s_branch .LBB0_897

.LBB0_969:
	s_waitcnt vmcnt(0)
.LBB0_970:
	s_or_b64 exec, exec, s[0:1]
	s_waitcnt lgkmcnt(0)
	s_barrier
	s_getreg_b32 s0, hwreg(HW_REG_HW_ID, 0, 6)
	s_lshl_b32 s0, s0, 2
	s_add_i32 s0, s0, 0x27000
	v_mov_b32_e32 v0, s0
	ds_read_b32 v0, v0
	v_mov_b32_e32 v1, 0
	v_mov_b32_e32 v4, 0
	s_waitcnt lgkmcnt(0)
	v_readfirstlane_b32 s0, v0
	v_mbcnt_lo_u32_b32 v0, -1, v1
	v_mbcnt_hi_u32_b32 v0, -1, v0
	v_lshl_or_b32 v2, s0, 6, v0
	s_getreg_b32 s0, hwreg(HW_REG_HW_ID, 0, 6)
	s_lshl_b32 s0, s0, 2
	s_add_i32 s0, s0, 0x27000
	v_mov_b32_e32 v0, s0
	ds_read_b32 v0, v0
	v_mov_b32_e32 v1, 0
	s_waitcnt lgkmcnt(0)
	v_readfirstlane_b32 s0, v0
	v_mbcnt_lo_u32_b32 v0, -1, v1
	v_mbcnt_hi_u32_b32 v0, -1, v0
	v_lshl_or_b32 v3, s0, 6, v0
	s_getreg_b32 s0, hwreg(HW_REG_HW_ID, 0, 6)
	s_lshl_b32 s0, s0, 2
	s_add_i32 s0, s0, 0x27000
	v_mov_b32_e32 v0, s0
	ds_read_b32 v0, v0
	v_mov_b32_e32 v1, 0
	s_waitcnt lgkmcnt(0)
	v_readfirstlane_b32 s0, v0
	v_mbcnt_lo_u32_b32 v0, -1, v4
	v_mbcnt_hi_u32_b32 v0, -1, v0
	v_lshl_or_b32 v0, s0, 6, v0
	s_movk_i32 s0, 0x100
	s_nop 0
	v_cmp_gt_i32_e32 vcc, s0, v0
	v_lshl_add_u32 v4, v0, 2, 0
	v_ashrrev_i32_e32 v0, 6, v3
	v_readlane_b32 s0, v253, 30
	s_waitcnt lgkmcnt(0)
	s_barrier
	v_add_u32_e32 v80, s0, v0
	s_movk_i32 s0, 0x4000
	v_cmp_gt_i32_e32 vcc, s0, v80
	s_and_saveexec_b64 s[2:3], vcc
	s_cbranch_execz .LBB0_1014
	v_readlane_b32 s4, v253, 4
	v_and_b32_e32 v1, 63, v2
	v_readlane_b32 s5, v253, 5
	v_lshlrev_b32_e32 v2, 5, v1
	v_mov_b32_e32 v3, 0
	v_readlane_b32 s18, v253, 18
	v_readlane_b32 s19, v253, 19
	v_readlane_b32 s4, v254, 3
	v_lshl_add_u64 v[84:85], s[64:65], 0, v[2:3]
	v_lshl_add_u64 v[82:83], s[18:19], 0, v[2:3]
	v_lshlrev_b32_e32 v2, 4, v1
	v_readlane_b32 s5, v254, 4
	v_lshlrev_b32_e32 v0, 3, v0
	v_ashrrev_i32_e32 v81, 31, v80
	v_lshl_add_u64 v[86:87], s[4:5], 0, v[2:3]
	s_lshl_b32 s4, s72, 6
	v_cmp_gt_u32_e64 s[0:1], 8, v1
	v_add3_u32 v88, s4, v0, v1
	v_readlane_b32 s4, v253, 2
	v_lshlrev_b64 v[0:1], 11, v[80:81]
	v_readlane_b32 s9, v253, 9
	v_readlane_b32 s5, v253, 3
	v_or_b32_e32 v0, v0, v2
	v_readlane_b32 s6, v253, 6
	v_readlane_b32 s7, v253, 7
	v_readlane_b32 s8, v253, 8
	s_lshl_b32 s9, s4, 6
	v_lshl_add_u64 v[0:1], s[70:71], 0, v[0:1]
	s_mov_b64 s[4:5], 0xd60d500
	s_ashr_i32 s75, s74, 31
	v_lshl_add_u64 v[90:91], v[0:1], 0, s[4:5]
	s_lshl_b64 s[4:5], s[74:75], 11
	s_mov_b64 s[6:7], 0
	s_mov_b32 s8, 0x3fb504f3
	v_mov_b32_e32 v81, 0x3727c5ac
	v_readlane_b32 s10, v253, 10
	v_readlane_b32 s11, v253, 11
	v_readlane_b32 s12, v253, 12
	v_readlane_b32 s13, v253, 13
	v_readlane_b32 s14, v253, 14
	v_readlane_b32 s15, v253, 15
	v_readlane_b32 s16, v253, 16
	v_readlane_b32 s17, v253, 17
	v_min_u32_e32 v240, 0x1ffff, v88
	v_mov_b32_e32 v241, 0
	v_readlane_b32 s98, v253, 55
	v_readlane_b32 s99, v253, 56
	v_lshlrev_b64 v[240:241], 2, v[240:241]
	s_nop 1
	v_lshl_add_u64 v[242:243], s[98:99], 0, v[240:241]
	global_load_dword v244, v[242:243], off
	v_readlane_b32 s98, v253, 59
	v_readlane_b32 s99, v253, 60
	s_nop 1
	v_lshl_add_u64 v[242:243], s[98:99], 0, v[240:241]
	global_load_dword v245, v[242:243], off
	v_readlane_b32 s98, v253, 57
	v_readlane_b32 s99, v253, 58
	s_nop 1
	v_lshl_add_u64 v[242:243], s[98:99], 0, v[240:241]
	global_load_dword v246, v[242:243], off
	global_load_dwordx4 v[200:203], v[82:83], off
	global_load_dwordx4 v[204:207], v[82:83], off offset:16
	global_load_dwordx4 v[208:211], v[84:85], off
	global_load_dwordx4 v[212:215], v[84:85], off offset:16
	global_load_dwordx4 v[216:219], v[82:83], off offset:2048
	global_load_dwordx4 v[220:223], v[82:83], off offset:2064
	global_load_dwordx4 v[224:227], v[84:85], off offset:2048
	global_load_dwordx4 v[228:231], v[84:85], off offset:2064
	s_waitcnt vmcnt(0)
	s_branch .LBB0_1012

.LBB0_1065:
	s_waitcnt vmcnt(0)
.LBB0_1066:
	s_or_b64 exec, exec, s[0:1]
	s_waitcnt lgkmcnt(0)
	s_barrier
	s_getreg_b32 s0, hwreg(HW_REG_HW_ID, 0, 6)
	s_lshl_b32 s0, s0, 2
	s_add_i32 s0, s0, 0x27000
	v_mov_b32_e32 v0, s0
	ds_read_b32 v0, v0
	v_mov_b32_e32 v1, 0
	s_cmpk_lt_i32 s72, 0x2c0
	s_cselect_b64 s[2:3], -1, 0
	s_waitcnt lgkmcnt(0)
	v_readfirstlane_b32 s0, v0
	v_mbcnt_lo_u32_b32 v0, -1, v1
	v_mbcnt_hi_u32_b32 v0, -1, v0
	s_waitcnt vmcnt(10)
	v_lshl_or_b32 v14, s0, 6, v0
	s_cmpk_gt_i32 s72, 0x2bf
	v_readfirstlane_b32 s44, v14
	s_cbranch_scc1 .LBB0_1068
	s_ashr_i32 s0, s72, 31
	s_lshr_b32 s0, s0, 29
	s_add_i32 s0, s72, s0
	s_ashr_i32 s1, s0, 3
	s_and_b32 s0, s0, -8
	s_sub_i32 s0, s72, s0
	s_cmp_lt_i32 s0, 0
	s_movk_i32 s4, 0x59
	s_cselect_b32 s4, s4, 0x58
	s_mul_i32 s0, s4, s0
	s_add_i32 s0, s0, s1
	s_mul_hi_i32 s1, s0, 0x2e8ba2e9
	s_lshr_b32 s4, s1, 31
	s_ashr_i32 s1, s1, 4
	s_add_i32 s1, s1, s4
	s_lshl_b32 s4, s1, 3
	s_mulk_i32 s1, 0x58
	s_sub_i32 s0, s0, s1
	s_bfe_i32 s1, s0, 0x80000
	s_bfe_u32 s1, s1, 0x3000c
	s_add_i32 s1, s0, s1
	s_bfe_i32 s5, s1, 0x80000
	s_and_b32 s1, s1, 0xf8
	s_sub_i32 s0, s0, s1
	s_sext_i32_i16 s5, s5
	s_sext_i32_i8 s0, s0
	s_add_i32 s0, s4, s0
	s_ashr_i32 s28, s5, 3

.LBB0_1451:
	s_waitcnt vmcnt(0)
.LBB0_1452:
	s_or_b64 exec, exec, s[0:1]
	s_add_u32 s0, s70, 0x2e18d500
	s_addc_u32 s1, s71, 0
	v_writelane_b32 v254, s0, 5
	s_cmp_gt_i32 s72, 63
	s_waitcnt lgkmcnt(0)
	v_writelane_b32 v254, s1, 6
	s_barrier
	s_cbranch_scc1 .LBB0_1587
	s_add_u32 s2, s70, 0x2df8d500
	v_readlane_b32 s0, v253, 2
	s_addc_u32 s3, s71, 0
	s_lshl_b32 s14, s72, 7
	s_lshl_b32 s15, s0, 7
	s_mov_b32 s5, 0
	v_mov_b32_e32 v65, 0
	s_movk_i32 s16, 0xff
	v_mov_b32_e32 v74, 0xfe0
	s_movk_i32 s17, 0xf000
	s_movk_i32 s18, 0x1400
	s_movk_i32 s19, 0x2000
	s_movk_i32 s20, 0x4000
	s_movk_i32 s21, 0x6000
	s_movk_i32 s22, 0x90
	s_add_i32 s23, 0, 0x16800
	s_movk_i32 s24, 0x1000
	s_mov_b32 s25, 0xfffffe0
	s_add_i32 s26, 0, 0x1a800
	s_mov_b32 s27, 0x210f000
	s_mov_b32 s28, 0x2111000
	s_mov_b64 s[6:7], 0x2800
	s_mov_b32 s29, 0x3f200000
	s_mov_b32 s33, 0x3fb8aa3b
	s_mov_b32 s36, 0xc2ce8ed0
	s_mov_b32 s37, 0x42b17218
	v_mov_b32_e32 v75, 0x3ca908c9
	s_brev_b32 s38, -2
	v_mov_b32_e32 v76, 4
	v_mov_b32_e32 v77, 0x7f800000
	s_mov_b32 s39, s72
	v_readlane_b32 s1, v253, 3
	s_branch .LBB0_1455

.LBB0_1638:
	s_waitcnt vmcnt(0)
.LBB0_1639:
	s_or_b64 exec, exec, s[0:1]
	s_cmpk_gt_i32 s72, 0x3ff
	s_waitcnt lgkmcnt(0)
	s_barrier
	s_cbranch_scc1 .LBB0_1851
	v_writelane_b32 v254, s68, 7
	s_add_u32 s84, s70, 0x2e28d500
	v_writelane_b32 v254, s64, 8
	s_addc_u32 s85, s71, 0
	s_bitcmp1_b32 s72, 0
	v_writelane_b32 v254, s65, 9
	v_readlane_b32 s0, v253, 2
	v_writelane_b32 v254, s66, 10
	s_cselect_b64 s[78:79], -1, 0
	v_readlane_b32 s1, v253, 3
	s_bitcmp1_b32 s0, 0
	v_writelane_b32 v254, s67, 11
	s_cselect_b64 s[0:1], -1, 0
	v_writelane_b32 v254, s0, 12
	s_mov_b32 s80, s72
	s_movk_i32 s75, 0xc0
	v_writelane_b32 v254, s1, 13
	v_readlane_b32 s0, v253, 22
	v_readlane_b32 s1, v253, 23
	s_add_i32 s86, 0, 0x8800
	v_mov_b32_e32 v177, 0
	v_mov_b64_e32 v[178:179], s[0:1]
	s_add_i32 s0, 0, 0x18c00
	v_writelane_b32 v254, s0, 14
	v_writelane_b32 v254, s70, 15
	s_movk_i32 s67, 0xff
	s_mov_b32 s65, 0
	v_writelane_b32 v254, s71, 16
	v_writelane_b32 v254, s72, 17
	s_movk_i32 s25, 0x1400
	s_mov_b32 s66, 0x3e38aa3b
	v_writelane_b32 v254, s73, 18
	v_writelane_b32 v254, s74, 19
	s_movk_i32 s87, 0x2080
	s_mov_b32 s33, 0xbffffffe
	v_writelane_b32 v254, s75, 20
	v_writelane_b32 v254, s92, 21
	v_mov_b32_e32 v181, 0xff800000
	v_mov_b32_e32 v190, 0x461c4000
	v_writelane_b32 v254, s93, 22
	v_writelane_b32 v254, s76, 23
	v_mov_b32_e32 v191, 0x28000
	v_bfrev_b32_e32 v192, 1
	v_writelane_b32 v254, s77, 24
	v_writelane_b32 v254, s84, 25
	s_nop 1
	v_writelane_b32 v254, s85, 26
	v_writelane_b32 v254, s86, 27
	s_branch .LBB0_1643

.LBB0_1902:
	s_waitcnt vmcnt(0)
.LBB0_1903:
	s_or_b64 exec, exec, s[0:1]
	v_readlane_b32 s0, v253, 31
	v_readlane_b32 s6, v253, 37
	v_readlane_b32 s10, v253, 41
	v_readlane_b32 s2, v253, 33
	v_readlane_b32 s3, v253, 34
	v_readlane_b32 s7, v253, 38
	v_readlane_b32 s11, v253, 42
	s_add_u32 s6, s10, 0x1000
	v_readlane_b32 s8, v253, 39
	v_readlane_b32 s12, v253, 43
	s_addc_u32 s7, s11, 0
	v_readlane_b32 s2, v253, 24
	v_readlane_b32 s1, v253, 32
	v_readlane_b32 s9, v253, 40
	v_readlane_b32 s13, v253, 44
	s_add_u32 s8, s12, 0x1000
	v_readlane_b32 s3, v253, 25
	s_addc_u32 s9, s13, 0
	s_mov_b64 s[0:1], -1
	s_and_b64 vcc, exec, s[2:3]
	s_waitcnt lgkmcnt(0)
	s_barrier
	v_readlane_b32 s4, v253, 35
	v_readlane_b32 s5, v253, 36
	v_readlane_b32 s14, v253, 45
	v_readlane_b32 s15, v253, 46
	s_cbranch_vccz .LBB0_1984
	s_getreg_b32 s0, hwreg(HW_REG_HW_ID, 0, 6)
	s_lshl_b32 s0, s0, 2
	s_add_i32 s0, s0, 0x27000
	v_mov_b32_e32 v0, s0
	ds_read_b32 v0, v0
	v_mov_b32_e32 v1, 0
	v_mov_b32_e32 v133, 0
	v_mbcnt_lo_u32_b32 v1, -1, v1
	s_waitcnt lgkmcnt(0)
	v_readfirstlane_b32 s0, v0
	v_mbcnt_hi_u32_b32 v0, -1, v1
	s_cmpk_gt_i32 s72, 0xff
	v_lshl_or_b32 v8, s0, 6, v0
	s_nop 0
	v_readfirstlane_b32 s3, v8
	s_cbranch_scc1 .LBB0_1924
	s_ashr_i32 s26, s72, 31
	s_lshr_b32 s0, s26, 29
	s_add_i32 s5, s72, s0
	s_and_b32 s0, s5, -8
	s_sub_i32 s4, s72, s0
	s_cmp_gt_i32 s4, -1
	s_cbranch_scc0 .LBB0_1907
	s_lshl_b32 s2, s4, 5
	s_ashr_i32 s1, s5, 3
	s_cbranch_execz .LBB0_1908
	s_branch .LBB0_1909

.LBB0_1975:
	s_waitcnt vmcnt(0)
.LBB0_1976:
	s_or_b64 exec, exec, s[0:1]
	s_waitcnt lgkmcnt(0)
	s_barrier
	s_getreg_b32 s0, hwreg(HW_REG_HW_ID, 0, 6)
	s_lshl_b32 s0, s0, 2
	s_add_i32 s0, s0, 0x27000
	v_mov_b32_e32 v0, s0
	ds_read_b32 v0, v0
	v_mov_b32_e32 v1, 0
	s_movk_i32 s24, 0x4000
	v_mov_b32_e32 v33, 0
	s_waitcnt lgkmcnt(0)
	v_readfirstlane_b32 s0, v0
	v_mbcnt_lo_u32_b32 v0, -1, v1
	v_mbcnt_hi_u32_b32 v0, -1, v0
	v_lshl_or_b32 v34, s0, 6, v0
	s_getreg_b32 s0, hwreg(HW_REG_HW_ID, 0, 6)
	s_lshl_b32 s0, s0, 2
	s_add_i32 s0, s0, 0x27000
	v_mov_b32_e32 v0, s0
	ds_read_b32 v0, v0
	v_mov_b32_e32 v1, 0
	s_waitcnt lgkmcnt(0)
	v_readfirstlane_b32 s0, v0
	v_mbcnt_lo_u32_b32 v0, -1, v1
	v_mbcnt_hi_u32_b32 v0, -1, v0
	v_lshl_or_b32 v0, s0, 6, v0
	v_readlane_b32 s0, v253, 30
	v_ashrrev_i32_e32 v0, 6, v0
	s_nop 0
	v_add_u32_e32 v80, s0, v0
	v_cmp_gt_i32_e32 vcc, s24, v80
	s_and_saveexec_b64 s[10:11], vcc
	s_cbranch_execz .LBB0_1983
	v_lshlrev_b32_e32 v0, 3, v34
	v_and_b32_e32 v35, 0x1f8, v0
	v_lshlrev_b32_e32 v32, 2, v35
	v_or_b32_e32 v28, 0x800, v32
	global_load_dwordx4 v[0:3], v32, s[6:7] offset:16
	global_load_dwordx4 v[4:7], v32, s[6:7]
	global_load_dwordx4 v[8:11], v32, s[8:9] offset:16
	global_load_dwordx4 v[12:15], v32, s[8:9]
	global_load_dwordx4 v[16:19], v28, s[6:7] offset:16
	global_load_dwordx4 v[20:23], v28, s[6:7]
	global_load_dwordx4 v[24:27], v28, s[8:9] offset:16
	s_nop 0
	global_load_dwordx4 v[28:31], v28, s[8:9]
	v_readlane_b32 s2, v253, 49
	v_readlane_b32 s3, v253, 50
	v_ashrrev_i32_e32 v81, 31, v80
	v_lshlrev_b64 v[90:91], 12, v[80:81]
	v_lshl_add_u64 v[82:83], s[2:3], 0, v[32:33]
	v_readlane_b32 s2, v253, 51
	v_lshlrev_b32_e32 v32, 1, v35
	v_readlane_b32 s3, v253, 52
	v_lshl_add_u64 v[84:85], s[92:93], 0, v[32:33]
	v_readlane_b32 s0, v253, 2
	v_lshl_add_u64 v[86:87], s[2:3], 0, v[32:33]
	v_and_b32_e32 v32, 63, v34
	v_lshlrev_b32_e32 v34, 4, v32
	v_lshl_or_b32 v90, v32, 5, v90
	v_add_u32_e32 v32, s74, v80
	s_lshl_b32 s12, s0, 5
	v_ashrrev_i32_e32 v33, 31, v32
	v_lshlrev_b64 v[88:89], 11, v[80:81]
	s_ashr_i32 s13, s12, 31
	v_lshlrev_b64 v[92:93], 11, v[32:33]
	v_or_b32_e32 v88, v88, v34
	s_lshl_b64 s[14:15], s[12:13], 11
	s_lshl_b64 s[16:17], s[12:13], 12
	s_lshl_b32 s13, s0, 4
	s_mul_i32 s25, s0, 24
	v_or_b32_e32 v92, v92, v34
	s_mov_b64 s[18:19], 0
	s_mov_b64 s[20:21], 0x960d500
	s_mov_b64 s[22:23], 0x960dd00
	s_mov_b32 s26, 0x960d000
	v_mov_b32_e32 v81, 0x3727c5ac
	s_mov_b32 s27, 0x800000
	s_mov_b32 s28, 0xd60d000
	s_mov_b32 s29, 0xf60d000
	s_movk_i32 s30, 0x3fff
	v_readlane_b32 s1, v253, 3
	s_branch .LBB0_1979

.LBB0_2100:
	s_waitcnt vmcnt(0)
.LBB0_2101:
	s_or_b64 exec, exec, s[0:1]
	s_waitcnt lgkmcnt(0)
	s_barrier
	s_getreg_b32 s0, hwreg(HW_REG_HW_ID, 0, 6)
	s_lshl_b32 s0, s0, 2
	s_add_i32 s0, s0, 0x27000
	v_mov_b32_e32 v0, s0
	ds_read_b32 v0, v0
	v_mov_b32_e32 v1, 0
	s_movk_i32 s7, 0x100
	s_mov_b32 s6, s72
	s_waitcnt lgkmcnt(0)
	v_readfirstlane_b32 s0, v0
	v_mbcnt_lo_u32_b32 v0, -1, v1
	v_mbcnt_hi_u32_b32 v0, -1, v0
	v_lshl_or_b32 v0, s0, 6, v0
	v_readlane_b32 s0, v253, 63
	v_readlane_b32 s1, v254, 0
	s_and_b64 vcc, exec, s[0:1]
	v_readlane_b32 s0, v253, 2
	s_mov_b32 s8, s0
	v_readlane_b32 s1, v253, 3
	s_cbranch_vccz .LBB0_2103
	s_cmp_ge_i32 s6, s7
	s_cbranch_scc0 .LBB0_2104
	s_branch .LBB0_2108

.LBB0_2159:
	s_waitcnt vmcnt(0)
.LBB0_2160:
	s_or_b64 exec, exec, s[0:1]
	s_waitcnt lgkmcnt(0)
	s_barrier
	s_add_u32 s30, s70, 0x9440
	s_getreg_b32 s0, hwreg(HW_REG_HW_ID, 0, 6)
	s_addc_u32 s31, s71, 0
	s_lshl_b32 s0, s0, 2
	s_add_i32 s0, s0, 0x27000
	v_mov_b32_e32 v0, s0
	ds_read_b32 v0, v0
	v_mov_b32_e32 v1, 0
	v_mov_b32_e32 v3, 0
	s_movk_i32 s33, 0x4000
	s_waitcnt lgkmcnt(0)
	v_readfirstlane_b32 s0, v0
	v_mbcnt_lo_u32_b32 v0, -1, v1
	v_mbcnt_hi_u32_b32 v0, -1, v0
	v_lshl_or_b32 v0, s0, 6, v0
	s_getreg_b32 s0, hwreg(HW_REG_HW_ID, 0, 6)
	s_lshl_b32 s0, s0, 2
	s_add_i32 s0, s0, 0x27000
	v_mov_b32_e32 v1, s0
	ds_read_b32 v2, v1
	v_mov_b32_e32 v1, 0
	s_waitcnt lgkmcnt(0)
	v_readfirstlane_b32 s0, v2
	v_mbcnt_lo_u32_b32 v2, -1, v3
	v_mbcnt_hi_u32_b32 v2, -1, v2
	v_lshl_or_b32 v2, s0, 6, v2
	v_readlane_b32 s0, v253, 30
	v_ashrrev_i32_e32 v8, 6, v2
	s_nop 0
	v_add_u32_e32 v2, s0, v8
	v_cmp_gt_i32_e32 vcc, s33, v2
	s_and_saveexec_b64 s[34:35], vcc
	s_cbranch_execz .LBB0_2249
	v_ashrrev_i32_e32 v3, 31, v2
	v_readlane_b32 s24, v253, 53
	v_and_b32_e32 v22, 63, v0
	v_lshlrev_b64 v[4:5], 10, v[2:3]
	v_readlane_b32 s25, v253, 54
	v_lshlrev_b32_e32 v0, 2, v22
	v_readlane_b32 s8, v253, 4
	v_lshl_add_u64 v[4:5], s[24:25], 0, v[4:5]
	v_lshl_add_u64 v[4:5], v[4:5], 0, v[0:1]
	global_load_dword v28, v[4:5], off
	global_load_dword v29, v[4:5], off offset:256
	global_load_dword v30, v[4:5], off offset:512
	global_load_dword v31, v[4:5], off offset:768
	v_readlane_b32 s9, v253, 5
	v_xor_b32_e32 v3, 64, v0
	v_xor_b32_e32 v23, 0x80, v0
	v_lshl_add_u64 v[4:5], s[8:9], 0, v[0:1]
	global_load_dword v61, v[4:5], off offset:1024
	global_load_dword v62, v[4:5], off offset:1280
	global_load_dword v63, v[4:5], off offset:1536
	global_load_dword v64, v[4:5], off offset:1792
	v_lshl_add_u64 v[6:7], s[24:25], 0, v[0:1]
	s_lshl_b32 s24, s72, 6
	v_lshlrev_b32_e32 v0, 3, v8
	v_readlane_b32 s10, v253, 6
	v_readlane_b32 s11, v253, 7
	v_readlane_b32 s12, v253, 8
	v_readlane_b32 s13, v253, 9
	v_readlane_b32 s14, v253, 10
	v_readlane_b32 s15, v253, 11
	v_readlane_b32 s16, v253, 12
	v_readlane_b32 s17, v253, 13
	v_readlane_b32 s18, v253, 14
	v_readlane_b32 s19, v253, 15
	v_readlane_b32 s20, v253, 16
	v_readlane_b32 s21, v253, 17
	v_readlane_b32 s22, v253, 18
	v_readlane_b32 s23, v253, 19
	v_add3_u32 v8, s24, v0, v22
	v_readlane_b32 s24, v253, 2
	v_cmp_gt_u32_e64 s[0:1], 32, v22
	v_cmp_lt_u32_e64 s[2:3], 31, v22
	v_cmp_lt_u32_e64 s[4:5], 7, v22
	v_cmp_gt_u32_e64 s[6:7], 8, v22
	v_cmp_eq_u32_e64 s[8:9], 0, v22
	v_cmp_eq_u32_e64 s[10:11], 1, v22
	v_cmp_eq_u32_e64 s[12:13], 2, v22
	v_cmp_eq_u32_e64 s[14:15], 3, v22
	v_cmp_eq_u32_e64 s[16:17], 4, v22
	v_cmp_eq_u32_e64 s[18:19], 5, v22
	v_cmp_eq_u32_e64 s[20:21], 6, v22
	v_cmp_eq_u32_e64 s[22:23], 7, v22
	s_lshl_b32 s42, s24, 6
	s_mov_b64 s[36:37], 0
	s_movk_i32 s43, 0x3fff
	s_mov_b32 s44, 0xbfb8aa3b
	s_mov_b32 s45, 0x42ce8ed0
	s_mov_b32 s46, 0xc2b17218
	v_mov_b32_e32 v24, 0x7f800000
	v_mov_b32_e32 v25, 0xff800000
	s_mov_b32 s47, 0xff800000
	v_mov_b32_e32 v26, 1
	v_readlane_b32 s25, v253, 3
	s_waitcnt vmcnt(0)
	s_branch .LBB0_2163

.LBB0_2300:
	s_waitcnt vmcnt(0)
.LBB0_2301:
	s_or_b64 exec, exec, s[0:1]
	s_waitcnt lgkmcnt(0)
	s_barrier
	s_getreg_b32 s0, hwreg(HW_REG_HW_ID, 0, 6)
	s_lshl_b32 s0, s0, 2
	s_add_i32 s0, s0, 0x27000
	v_mov_b32_e32 v0, s0
	ds_read_b32 v0, v0
	v_mov_b32_e32 v1, 0
	v_mov_b32_e32 v2, 0
	s_waitcnt lgkmcnt(0)
	v_readfirstlane_b32 s0, v0
	v_mbcnt_lo_u32_b32 v0, -1, v1
	v_mbcnt_hi_u32_b32 v0, -1, v0
	s_waitcnt vmcnt(9)
	v_lshl_or_b32 v52, s0, 6, v0
	s_getreg_b32 s0, hwreg(HW_REG_HW_ID, 0, 6)
	s_lshl_b32 s0, s0, 2
	s_add_i32 s0, s0, 0x27000
	v_mov_b32_e32 v0, s0
	ds_read_b32 v0, v0
	v_mov_b32_e32 v1, 0
	s_waitcnt lgkmcnt(0)
	v_readfirstlane_b32 s0, v0
	v_mbcnt_lo_u32_b32 v0, -1, v2
	v_mbcnt_hi_u32_b32 v0, -1, v0
	v_lshl_or_b32 v0, s0, 6, v0
	s_movk_i32 s0, 0x100
	s_nop 0
	v_cmp_gt_i32_e32 vcc, s0, v0
	v_lshl_add_u32 v2, v0, 2, 0
	s_and_saveexec_b64 s[0:1], vcc
	s_cbranch_execz .LBB0_2303
	v_ashrrev_i32_e32 v1, 31, v0
	v_lshlrev_b32_e32 v4, 6, v0
	v_and_b32_e32 v4, 0xffffff00, v4
	v_and_b32_e32 v5, 3, v0
	v_lshl_or_b32 v4, v5, 5, v4
	v_mov_b32_e32 v5, 0
	v_lshl_add_u64 v[4:5], v[4:5], 0, s[30:31]
	global_load_dword v1, v[4:5], off
	v_add_u32_e32 v3, 0x1e800, v2
	s_mov_b32 s2, 0x66666667
	s_waitcnt vmcnt(0)
	ds_write_b32 v3, v1
	v_add_u32_e32 v3, 0x13f, v1
	v_mul_hi_i32 v3, v3, s2
	v_lshrrev_b32_e32 v4, 31, v3
	v_lshrrev_b32_e32 v3, 7, v3
	v_add_u32_e32 v3, v3, v4
	v_lshl_or_b32 v1, v3, 20, v1
	v_add_u32_e32 v3, 0x1ec10, v2
	ds_write_b32 v3, v1

.LBB0_2434:
	s_waitcnt vmcnt(0)
.LBB0_2435:
	s_or_b64 exec, exec, s[0:1]
	s_waitcnt lgkmcnt(0)
	s_barrier
	s_getreg_b32 s0, hwreg(HW_REG_HW_ID, 0, 6)
	s_lshl_b32 s0, s0, 2
	s_add_i32 s0, s0, 0x27000
	v_mov_b32_e32 v0, s0
	ds_read_b32 v0, v0
	v_mov_b32_e32 v1, 0
	v_mov_b32_e32 v2, 0
	s_waitcnt lgkmcnt(0)
	v_readfirstlane_b32 s0, v0
	v_mbcnt_lo_u32_b32 v0, -1, v1
	v_mbcnt_hi_u32_b32 v0, -1, v0
	v_lshl_or_b32 v52, s0, 6, v0
	s_getreg_b32 s0, hwreg(HW_REG_HW_ID, 0, 6)
	s_lshl_b32 s0, s0, 2
	s_add_i32 s0, s0, 0x27000
	v_mov_b32_e32 v0, s0
	ds_read_b32 v0, v0
	v_mov_b32_e32 v1, 0
	s_waitcnt lgkmcnt(0)
	v_readfirstlane_b32 s0, v0
	v_mbcnt_lo_u32_b32 v0, -1, v2
	v_mbcnt_hi_u32_b32 v0, -1, v0
	v_lshl_or_b32 v0, s0, 6, v0
	s_movk_i32 s0, 0x100
	s_nop 0
	v_cmp_gt_i32_e32 vcc, s0, v0
	v_lshl_add_u32 v2, v0, 2, 0
	s_add_i32 s0, 0, 0x1f424
	v_mov_b32_e32 v0, s0
	s_waitcnt lgkmcnt(0)
	s_barrier
	ds_read_b32 v0, v0
	v_readlane_b32 s2, v253, 63
	v_readlane_b32 s3, v254, 0
	s_and_b64 vcc, exec, s[2:3]
	s_waitcnt lgkmcnt(0)
	v_readfirstlane_b32 s0, v0
	s_lshl_b32 s0, s0, 3
	s_cbranch_vccz .LBB0_2476
	v_readlane_b32 s2, v253, 2
	s_mov_b32 s12, s72
	v_readlane_b32 s3, v253, 3
	s_mov_b32 s1, s2
	s_cmp_ge_i32 s12, s0
	s_cbranch_scc0 .LBB0_2477
	s_branch .LBB0_2497

.LBB0_2548:
	s_waitcnt vmcnt(0)
.LBB0_2549:
	s_or_b64 exec, exec, s[0:1]
	s_waitcnt lgkmcnt(0)
	s_barrier
	s_getreg_b32 s0, hwreg(HW_REG_HW_ID, 0, 6)
	s_lshl_b32 s0, s0, 2
	s_add_i32 s0, s0, 0x27000
	v_mov_b32_e32 v0, s0
	ds_read_b32 v0, v0
	v_mov_b32_e32 v1, 0
	v_mov_b32_e32 v4, 0
	s_waitcnt lgkmcnt(0)
	v_readfirstlane_b32 s0, v0
	v_mbcnt_lo_u32_b32 v0, -1, v1
	v_mbcnt_hi_u32_b32 v0, -1, v0
	v_lshl_or_b32 v2, s0, 6, v0
	s_getreg_b32 s0, hwreg(HW_REG_HW_ID, 0, 6)
	s_lshl_b32 s0, s0, 2
	s_add_i32 s0, s0, 0x27000
	v_mov_b32_e32 v0, s0
	ds_read_b32 v0, v0
	v_mov_b32_e32 v1, 0
	s_waitcnt lgkmcnt(0)
	v_readfirstlane_b32 s0, v0
	v_mbcnt_lo_u32_b32 v0, -1, v1
	v_mbcnt_hi_u32_b32 v0, -1, v0
	v_lshl_or_b32 v3, s0, 6, v0
	s_getreg_b32 s0, hwreg(HW_REG_HW_ID, 0, 6)
	s_lshl_b32 s0, s0, 2
	s_add_i32 s0, s0, 0x27000
	v_mov_b32_e32 v0, s0
	ds_read_b32 v0, v0
	v_mov_b32_e32 v1, 0
	s_waitcnt lgkmcnt(0)
	v_readfirstlane_b32 s0, v0
	v_mbcnt_lo_u32_b32 v0, -1, v4
	v_mbcnt_hi_u32_b32 v0, -1, v0
	v_lshl_or_b32 v0, s0, 6, v0
	s_movk_i32 s0, 0x100
	s_nop 0
	v_cmp_gt_i32_e32 vcc, s0, v0
	v_lshl_add_u32 v4, v0, 2, 0
	v_ashrrev_i32_e32 v0, 6, v3
	v_readlane_b32 s0, v253, 30
	s_waitcnt lgkmcnt(0)
	s_barrier
	v_add_u32_e32 v24, s0, v0
	s_movk_i32 s0, 0x4000
	v_cmp_gt_i32_e32 vcc, s0, v24
	s_and_saveexec_b64 s[0:1], vcc
	s_cbranch_execz .LBB0_2595
	v_readlane_b32 s0, v253, 4
	v_readlane_b32 s2, v253, 6
	v_readlane_b32 s14, v253, 18
	v_readlane_b32 s3, v253, 7
	v_readlane_b32 s15, v253, 19
	s_add_u32 s2, s14, 0x1000
	v_and_b32_e32 v1, 63, v2
	v_readlane_b32 s6, v253, 10
	s_addc_u32 s3, s15, 0
	v_lshlrev_b32_e32 v2, 5, v1
	v_mov_b32_e32 v3, 0
	v_readlane_b32 s7, v253, 11
	s_add_u32 s6, s64, 0x1000
	v_or_b32_e32 v4, 0x800, v2
	v_mov_b32_e32 v5, v3
	s_addc_u32 s7, s65, 0
	v_lshl_add_u64 v[26:27], s[2:3], 0, v[2:3]
	v_lshl_add_u64 v[30:31], s[2:3], 0, v[4:5]
	v_readlane_b32 s2, v254, 3
	v_readlane_b32 s12, v253, 16
	v_readlane_b32 s13, v253, 17
	s_cmp_lg_u64 s[66:67], 0
	v_lshl_add_u64 v[32:33], s[6:7], 0, v[4:5]
	v_lshlrev_b32_e32 v4, 4, v1
	v_readlane_b32 s3, v254, 4
	v_readlane_b32 s1, v253, 5
	s_cselect_b64 s[12:13], -1, 0
	v_lshl_add_u64 v[34:35], s[2:3], 0, v[4:5]
	s_lshl_b32 s2, s72, 6
	v_lshlrev_b32_e32 v0, 3, v0
	v_ashrrev_i32_e32 v25, 31, v24
	v_cmp_gt_u32_e64 s[0:1], 8, v1
	v_add3_u32 v36, s2, v0, v1
	v_readlane_b32 s2, v253, 2
	v_lshlrev_b64 v[0:1], 11, v[24:25]
	v_readlane_b32 s11, v253, 15
	v_readlane_b32 s3, v253, 3
	v_or_b32_e32 v0, v0, v4
	s_lshl_b32 s11, s2, 6
	v_lshl_add_u64 v[0:1], s[70:71], 0, v[0:1]
	s_mov_b64 s[2:3], 0xd60d900
	v_lshl_add_u64 v[38:39], v[0:1], 0, s[2:3]
	v_lshlrev_b64 v[0:1], 12, v[24:25]
	v_or_b32_e32 v0, v0, v2
	v_lshl_add_u64 v[0:1], s[66:67], 0, v[0:1]
	s_mov_b64 s[2:3], 0x800
	v_readlane_b32 s4, v253, 8
	v_readlane_b32 s5, v253, 9
	v_readlane_b32 s8, v253, 12
	v_readlane_b32 s9, v253, 13
	v_readlane_b32 s10, v253, 14
	s_ashr_i32 s75, s74, 31
	v_lshl_add_u64 v[40:41], v[0:1], 0, s[2:3]
	v_cndmask_b32_e64 v0, 0, 1, s[12:13]
	s_mov_b64 s[4:5], 0
	v_lshl_add_u64 v[28:29], s[6:7], 0, v[2:3]
	s_lshl_b64 s[6:7], s[74:75], 11
	s_lshl_b64 s[8:9], s[74:75], 12
	s_mov_b32 s10, 0x3fb504f3
	v_mov_b32_e32 v25, 0x3727c5ac
	s_mov_b32 s15, 0x800000
	s_movk_i32 s17, 0x3fff
	v_cmp_ne_u32_e64 s[2:3], 1, v0
	v_min_u32_e32 v240, 0x1ffff, v36
	v_mov_b32_e32 v241, 0
	v_readlane_b32 s98, v253, 55
	v_readlane_b32 s99, v253, 56
	v_lshlrev_b64 v[240:241], 2, v[240:241]
	s_nop 1
	v_lshl_add_u64 v[242:243], s[98:99], 0, v[240:241]
	global_load_dword v244, v[242:243], off
	v_readlane_b32 s98, v253, 59
	v_readlane_b32 s99, v253, 60
	s_nop 1
	v_lshl_add_u64 v[242:243], s[98:99], 0, v[240:241]
	global_load_dword v245, v[242:243], off
	v_readlane_b32 s98, v253, 57
	v_readlane_b32 s99, v253, 58
	s_nop 1
	v_lshl_add_u64 v[242:243], s[98:99], 0, v[240:241]
	global_load_dword v246, v[242:243], off
	global_load_dwordx4 v[200:203], v[26:27], off
	global_load_dwordx4 v[204:207], v[28:29], off
	global_load_dwordx4 v[208:211], v[26:27], off offset:16
	global_load_dwordx4 v[212:215], v[28:29], off offset:16
	global_load_dwordx4 v[216:219], v[30:31], off
	global_load_dwordx4 v[220:223], v[32:33], off
	global_load_dwordx4 v[224:227], v[30:31], off offset:16
	global_load_dwordx4 v[228:231], v[32:33], off offset:16
	s_waitcnt vmcnt(0)
	s_branch .LBB0_2591

	.amdhsa_kernel _Z7k_fused5KArgs
		.amdhsa_group_segment_fixed_size 0
		.amdhsa_private_segment_fixed_size 0
		.amdhsa_kernarg_size 472
		.amdhsa_user_sgpr_count 2
		.amdhsa_user_sgpr_dispatch_ptr 0
		.amdhsa_user_sgpr_queue_ptr 0
		.amdhsa_user_sgpr_kernarg_segment_ptr 1
		.amdhsa_user_sgpr_dispatch_id 0
		.amdhsa_user_sgpr_kernarg_preload_length 0
		.amdhsa_user_sgpr_kernarg_preload_offset 0
		.amdhsa_user_sgpr_private_segment_size 0
		.amdhsa_uses_dynamic_stack 0
		.amdhsa_enable_private_segment 0
		.amdhsa_system_sgpr_workgroup_id_x 1
		.amdhsa_system_sgpr_workgroup_id_y 0
		.amdhsa_system_sgpr_workgroup_id_z 0
		.amdhsa_system_sgpr_workgroup_info 0
		.amdhsa_system_vgpr_workitem_id 0
		.amdhsa_next_free_vgpr 256
		.amdhsa_next_free_sgpr 102
		.amdhsa_accum_offset 256
		.amdhsa_reserve_vcc 1
		.amdhsa_float_round_mode_32 0
		.amdhsa_float_round_mode_16_64 0
		.amdhsa_float_denorm_mode_32 3
		.amdhsa_float_denorm_mode_16_64 3
		.amdhsa_dx10_clamp 1
		.amdhsa_ieee_mode 1
		.amdhsa_fp16_overflow 0
		.amdhsa_tg_split 0
		.amdhsa_exception_fp_ieee_invalid_op 0
		.amdhsa_exception_fp_denorm_src 0
		.amdhsa_exception_fp_ieee_div_zero 0
		.amdhsa_exception_fp_ieee_overflow 0
		.amdhsa_exception_fp_ieee_underflow 0
		.amdhsa_exception_fp_ieee_inexact 0
		.amdhsa_exception_int_div_zero 0
	.end_amdhsa_kernel

amdhsa.kernels:
  - .agpr_count:     0
    .args:
      - .offset:         0
        .size:           216
        .value_kind:     by_value
      - .offset:         216
        .size:           4
        .value_kind:     hidden_block_count_x
      - .offset:         220
        .size:           4
        .value_kind:     hidden_block_count_y
      - .offset:         224
        .size:           4
        .value_kind:     hidden_block_count_z
      - .offset:         228
        .size:           2
        .value_kind:     hidden_group_size_x
      - .offset:         230
        .size:           2
        .value_kind:     hidden_group_size_y
      - .offset:         232
        .size:           2
        .value_kind:     hidden_group_size_z
      - .offset:         234
        .size:           2
        .value_kind:     hidden_remainder_x
      - .offset:         236
        .size:           2
        .value_kind:     hidden_remainder_y
      - .offset:         238
        .size:           2
        .value_kind:     hidden_remainder_z
      - .offset:         256
        .size:           8
        .value_kind:     hidden_global_offset_x
      - .offset:         264
        .size:           8
        .value_kind:     hidden_global_offset_y
      - .offset:         272
        .size:           8
        .value_kind:     hidden_global_offset_z
      - .offset:         280
        .size:           2
        .value_kind:     hidden_grid_dims
      - .offset:         336
        .size:           4
        .value_kind:     hidden_dynamic_lds_size
    .group_segment_fixed_size: 0
    .kernarg_segment_align: 8
    .kernarg_segment_size: 472
    .language:       OpenCL C
    .language_version:
      - 2
      - 0
    .max_flat_workgroup_size: 512
    .name:           _Z7k_fused5KArgs
    .private_segment_fixed_size: 0
    .sgpr_count:     108
    .sgpr_spill_count: 150
    .symbol:         _Z7k_fused5KArgs.kd
    .uniform_work_group_size: 1
    .uses_dynamic_stack: false
    .vgpr_count:     256
    .vgpr_spill_count: 0
    .wavefront_size: 64
